# baseline (speedup 1.0000x reference)
amdhsa.kernels:
  - .agpr_count:     16
    .args:
      - .actual_access:  read_only
        .address_space:  global
        .offset:         0
        .size:           8
        .value_kind:     global_buffer
      - .actual_access:  read_only
        .address_space:  global
        .offset:         8
        .size:           8
        .value_kind:     global_buffer
      - .actual_access:  write_only
        .address_space:  global
        .offset:         16
        .size:           8
        .value_kind:     global_buffer
    .group_segment_fixed_size: 35840
    .kernarg_segment_align: 8
    .kernarg_segment_size: 24
    .language:       OpenCL C
    .language_version:
      - 2
      - 0
    .max_flat_workgroup_size: 256
    .name:           _Z6k_attnPKDF16_PKfPDF16_
    .private_segment_fixed_size: 0
    .sgpr_count:     16
    .sgpr_spill_count: 0
    .symbol:         _Z6k_attnPKDF16_PKfPDF16_.kd
    .uniform_work_group_size: 1
    .uses_dynamic_stack: false
    .vgpr_count:     84
    .vgpr_spill_count: 0
    .wavefront_size: 64
  - .agpr_count:     0
    .args:
      - .actual_access:  read_only
        .address_space:  global
        .offset:         0
        .size:           8
        .value_kind:     global_buffer
      - .actual_access:  read_only
        .address_space:  global
        .offset:         8
        .size:           8
        .value_kind:     global_buffer
      - .actual_access:  write_only
        .address_space:  global
        .offset:         16
        .size:           8
        .value_kind:     global_buffer
      - .actual_access:  write_only
        .address_space:  global
        .offset:         24
        .size:           8
        .value_kind:     global_buffer
      - .actual_access:  write_only
        .address_space:  global
        .offset:         32
        .size:           8
        .value_kind:     global_buffer
      - .actual_access:  write_only
        .address_space:  global
        .offset:         40
        .size:           8
        .value_kind:     global_buffer
    .group_segment_fixed_size: 0
    .kernarg_segment_align: 8
    .kernarg_segment_size: 48
    .language:       OpenCL C
    .language_version:
      - 2
      - 0
    .max_flat_workgroup_size: 256
    .name:           _Z11k_prep_miscPKiPKfPfPDv2_fS3_S3_
    .private_segment_fixed_size: 0
    .sgpr_count:     16
    .sgpr_spill_count: 0
    .symbol:         _Z11k_prep_miscPKiPKfPfPDv2_fS3_S3_.kd
    .uniform_work_group_size: 1
    .uses_dynamic_stack: false
    .vgpr_count:     6
    .vgpr_spill_count: 0
    .wavefront_size: 64
  - .agpr_count:     0
    .args:
      - .actual_access:  read_only
        .address_space:  global
        .offset:         0
        .size:           8
        .value_kind:     global_buffer
      - .actual_access:  write_only
        .address_space:  global
        .offset:         8
        .size:           8
        .value_kind:     global_buffer
    .group_segment_fixed_size: 0
    .kernarg_segment_align: 8
    .kernarg_segment_size: 16
    .language:       OpenCL C
    .language_version:
      - 2
      - 0
    .max_flat_workgroup_size: 256
    .name:           _Z7k_cvt_xPKfPDF16_
    .private_segment_fixed_size: 0
    .sgpr_count:     14
    .sgpr_spill_count: 0
    .symbol:         _Z7k_cvt_xPKfPDF16_.kd
    .uniform_work_group_size: 1
    .uses_dynamic_stack: false
    .vgpr_count:     12
    .vgpr_spill_count: 0
    .wavefront_size: 64
  - .agpr_count:     0
    .args:
      - .offset:         0
        .size:           176
        .value_kind:     by_value
    .group_segment_fixed_size: 9216
    .kernarg_segment_align: 8
    .kernarg_segment_size: 176
    .language:       OpenCL C
    .language_version:
      - 2
      - 0
    .max_flat_workgroup_size: 256
    .name:           _Z8k_wtrans8PrepArgs
    .private_segment_fixed_size: 0
    .sgpr_count:     44
    .sgpr_spill_count: 0
    .symbol:         _Z8k_wtrans8PrepArgs.kd
    .uniform_work_group_size: 1
    .uses_dynamic_stack: false
    .vgpr_count:     18
    .vgpr_spill_count: 0
    .wavefront_size: 64
  - .agpr_count:     0
    .args:
      - .offset:         0
        .size:           176
        .value_kind:     by_value
      - .actual_access:  read_only
        .address_space:  global
        .offset:         176
        .size:           8
        .value_kind:     global_buffer
      - .actual_access:  read_only
        .address_space:  global
        .offset:         184
        .size:           8
        .value_kind:     global_buffer
    .group_segment_fixed_size: 2048
    .kernarg_segment_align: 8
    .kernarg_segment_size: 192
    .language:       OpenCL C
    .language_version:
      - 2
      - 0
    .max_flat_workgroup_size: 256
    .name:           _Z8k_colvec8PrepArgsPKfS1_
    .private_segment_fixed_size: 0
    .sgpr_count:     38
    .sgpr_spill_count: 0
    .symbol:         _Z8k_colvec8PrepArgsPKfS1_.kd
    .uniform_work_group_size: 1
    .uses_dynamic_stack: false
    .vgpr_count:     114
    .vgpr_spill_count: 0
    .wavefront_size: 64
  - .agpr_count:     0
    .args:
      - .actual_access:  read_only
        .address_space:  global
        .offset:         0
        .size:           8
        .value_kind:     global_buffer
      - .actual_access:  write_only
        .address_space:  global
        .offset:         8
        .size:           8
        .value_kind:     global_buffer
    .group_segment_fixed_size: 0
    .kernarg_segment_align: 8
    .kernarg_segment_size: 16
    .language:       OpenCL C
    .language_version:
      - 2
      - 0
    .max_flat_workgroup_size: 256
    .name:           _Z9k_rowstatPKDv2_fPS_
    .private_segment_fixed_size: 0
    .sgpr_count:     16
    .sgpr_spill_count: 0
    .symbol:         _Z9k_rowstatPKDv2_fPS_.kd
    .uniform_work_group_size: 1
    .uses_dynamic_stack: false
    .vgpr_count:     28
    .vgpr_spill_count: 0
    .wavefront_size: 64
  - .agpr_count:     0
    .args:
      - .actual_access:  read_only
        .address_space:  global
        .offset:         0
        .size:           8
        .value_kind:     global_buffer
      - .actual_access:  read_only
        .address_space:  global
        .offset:         8
        .size:           8
        .value_kind:     global_buffer
      - .actual_access:  read_only
        .address_space:  global
        .offset:         16
        .size:           8
        .value_kind:     global_buffer
      - .actual_access:  read_only
        .address_space:  global
        .offset:         24
        .size:           8
        .value_kind:     global_buffer
      - .actual_access:  write_only
        .address_space:  global
        .offset:         32
        .size:           8
        .value_kind:     global_buffer
    .group_segment_fixed_size: 0
    .kernarg_segment_align: 8
    .kernarg_segment_size: 40
    .language:       OpenCL C
    .language_version:
      - 2
      - 0
    .max_flat_workgroup_size: 256
    .name:           _Z10k_final_lnPKDF16_PKDv2_fPKfS5_Pf
    .private_segment_fixed_size: 0
    .sgpr_count:     19
    .sgpr_spill_count: 0
    .symbol:         _Z10k_final_lnPKDF16_PKDv2_fPKfS5_Pf.kd
    .uniform_work_group_size: 1
    .uses_dynamic_stack: false
    .vgpr_count:     19
    .vgpr_spill_count: 0
    .wavefront_size: 64
  - .agpr_count:     0
    .args:
      - .offset:         0
        .size:           32
        .value_kind:     by_value
      - .offset:         32
        .size:           32
        .value_kind:     by_value
      - .offset:         64
        .size:           4
        .value_kind:     hidden_block_count_x
      - .offset:         68
        .size:           4
        .value_kind:     hidden_block_count_y
      - .offset:         72
        .size:           4
        .value_kind:     hidden_block_count_z
      - .offset:         76
        .size:           2
        .value_kind:     hidden_group_size_x
      - .offset:         78
        .size:           2
        .value_kind:     hidden_group_size_y
      - .offset:         80
        .size:           2
        .value_kind:     hidden_group_size_z
      - .offset:         82
        .size:           2
        .value_kind:     hidden_remainder_x
      - .offset:         84
        .size:           2
        .value_kind:     hidden_remainder_y
      - .offset:         86
        .size:           2
        .value_kind:     hidden_remainder_z
      - .offset:         104
        .size:           8
        .value_kind:     hidden_global_offset_x
      - .offset:         112
        .size:           8
        .value_kind:     hidden_global_offset_y
      - .offset:         120
        .size:           8
        .value_kind:     hidden_global_offset_z
      - .offset:         128
        .size:           2
        .value_kind:     hidden_grid_dims
      - .offset:         184
        .size:           4
        .value_kind:     hidden_dynamic_lds_size
    .group_segment_fixed_size: 0
    .kernarg_segment_align: 8
    .kernarg_segment_size: 320
    .language:       OpenCL C
    .language_version:
      - 2
      - 0
    .max_flat_workgroup_size: 512
    .name:           _Z6k_gemmIN2pg6EpiLinILi0EEELi768EEvNS0_4GemmET_
    .private_segment_fixed_size: 0
    .sgpr_count:     88
    .sgpr_spill_count: 0
    .symbol:         _Z6k_gemmIN2pg6EpiLinILi0EEELi768EEvNS0_4GemmET_.kd
    .uniform_work_group_size: 1
    .uses_dynamic_stack: false
    .vgpr_count:     256
    .vgpr_spill_count: 0
    .wavefront_size: 64
  - .agpr_count:     0
    .args:
      - .offset:         0
        .size:           32
        .value_kind:     by_value
      - .offset:         32
        .size:           56
        .value_kind:     by_value
      - .offset:         88
        .size:           4
        .value_kind:     hidden_block_count_x
      - .offset:         92
        .size:           4
        .value_kind:     hidden_block_count_y
      - .offset:         96
        .size:           4
        .value_kind:     hidden_block_count_z
      - .offset:         100
        .size:           2
        .value_kind:     hidden_group_size_x
      - .offset:         102
        .size:           2
        .value_kind:     hidden_group_size_y
      - .offset:         104
        .size:           2
        .value_kind:     hidden_group_size_z
      - .offset:         106
        .size:           2
        .value_kind:     hidden_remainder_x
      - .offset:         108
        .size:           2
        .value_kind:     hidden_remainder_y
      - .offset:         110
        .size:           2
        .value_kind:     hidden_remainder_z
      - .offset:         128
        .size:           8
        .value_kind:     hidden_global_offset_x
      - .offset:         136
        .size:           8
        .value_kind:     hidden_global_offset_y
      - .offset:         144
        .size:           8
        .value_kind:     hidden_global_offset_z
      - .offset:         152
        .size:           2
        .value_kind:     hidden_grid_dims
      - .offset:         208
        .size:           4
        .value_kind:     hidden_dynamic_lds_size
    .group_segment_fixed_size: 0
    .kernarg_segment_align: 8
    .kernarg_segment_size: 344
    .language:       OpenCL C
    .language_version:
      - 2
      - 0
    .max_flat_workgroup_size: 512
    .name:           _Z6k_gemmIN2pg6EpiResELi768EEvNS0_4GemmET_
    .private_segment_fixed_size: 0
    .sgpr_count:     108
    .sgpr_spill_count: 0
    .symbol:         _Z6k_gemmIN2pg6EpiResELi768EEvNS0_4GemmET_.kd
    .uniform_work_group_size: 1
    .uses_dynamic_stack: false
    .vgpr_count:     256
    .vgpr_spill_count: 0
    .wavefront_size: 64
  - .agpr_count:     0
    .args:
      - .offset:         0
        .size:           32
        .value_kind:     by_value
      - .offset:         32
        .size:           32
        .value_kind:     by_value
      - .offset:         64
        .size:           4
        .value_kind:     hidden_block_count_x
      - .offset:         68
        .size:           4
        .value_kind:     hidden_block_count_y
      - .offset:         72
        .size:           4
        .value_kind:     hidden_block_count_z
      - .offset:         76
        .size:           2
        .value_kind:     hidden_group_size_x
      - .offset:         78
        .size:           2
        .value_kind:     hidden_group_size_y
      - .offset:         80
        .size:           2
        .value_kind:     hidden_group_size_z
      - .offset:         82
        .size:           2
        .value_kind:     hidden_remainder_x
      - .offset:         84
        .size:           2
        .value_kind:     hidden_remainder_y
      - .offset:         86
        .size:           2
        .value_kind:     hidden_remainder_z
      - .offset:         104
        .size:           8
        .value_kind:     hidden_global_offset_x
      - .offset:         112
        .size:           8
        .value_kind:     hidden_global_offset_y
      - .offset:         120
        .size:           8
        .value_kind:     hidden_global_offset_z
      - .offset:         128
        .size:           2
        .value_kind:     hidden_grid_dims
      - .offset:         184
        .size:           4
        .value_kind:     hidden_dynamic_lds_size
    .group_segment_fixed_size: 0
    .kernarg_segment_align: 8
    .kernarg_segment_size: 320
    .language:       OpenCL C
    .language_version:
      - 2
      - 0
    .max_flat_workgroup_size: 512
    .name:           _Z6k_gemmIN2pg6EpiLinILi1EEELi768EEvNS0_4GemmET_
    .private_segment_fixed_size: 0
    .sgpr_count:     88
    .sgpr_spill_count: 0
    .symbol:         _Z6k_gemmIN2pg6EpiLinILi1EEELi768EEvNS0_4GemmET_.kd
    .uniform_work_group_size: 1
    .uses_dynamic_stack: false
    .vgpr_count:     256
    .vgpr_spill_count: 0
    .wavefront_size: 64
  - .agpr_count:     0
    .args:
      - .offset:         0
        .size:           32
        .value_kind:     by_value
      - .offset:         32
        .size:           56
        .value_kind:     by_value
      - .offset:         88
        .size:           4
        .value_kind:     hidden_block_count_x
      - .offset:         92
        .size:           4
        .value_kind:     hidden_block_count_y
      - .offset:         96
        .size:           4
        .value_kind:     hidden_block_count_z
      - .offset:         100
        .size:           2
        .value_kind:     hidden_group_size_x
      - .offset:         102
        .size:           2
        .value_kind:     hidden_group_size_y
      - .offset:         104
        .size:           2
        .value_kind:     hidden_group_size_z
      - .offset:         106
        .size:           2
        .value_kind:     hidden_remainder_x
      - .offset:         108
        .size:           2
        .value_kind:     hidden_remainder_y
      - .offset:         110
        .size:           2
        .value_kind:     hidden_remainder_z
      - .offset:         128
        .size:           8
        .value_kind:     hidden_global_offset_x
      - .offset:         136
        .size:           8
        .value_kind:     hidden_global_offset_y
      - .offset:         144
        .size:           8
        .value_kind:     hidden_global_offset_z
      - .offset:         152
        .size:           2
        .value_kind:     hidden_grid_dims
      - .offset:         208
        .size:           4
        .value_kind:     hidden_dynamic_lds_size
    .group_segment_fixed_size: 0
    .kernarg_segment_align: 8
    .kernarg_segment_size: 344
    .language:       OpenCL C
    .language_version:
      - 2
      - 0
    .max_flat_workgroup_size: 512
    .name:           _Z6k_gemmIN2pg6EpiResELi3072EEvNS0_4GemmET_
    .private_segment_fixed_size: 0
    .sgpr_count:     108
    .sgpr_spill_count: 0
    .symbol:         _Z6k_gemmIN2pg6EpiResELi3072EEvNS0_4GemmET_.kd
    .uniform_work_group_size: 1
    .uses_dynamic_stack: false
    .vgpr_count:     256
    .vgpr_spill_count: 0
    .wavefront_size: 64
